# P7 residual epilogue: 16 x-loads in flight instead of one serialized load-add-store chain, on top of the attention K-read hoist
# speedup vs baseline: 1.0117x; 1.0009x over previous
.LBB0_888:
	v_lshl_add_u32 v158, s30, 8, v146
	v_lshl_or_b32 v160, s60, 8, v147
	v_lshlrev_b32_e32 v248, 13, v158
	v_lshl_add_u32 v248, v160, 2, v248
	s_andn2_b64 vcc, exec, s[2:3]
	s_mov_b64 s[2:3], -1
	s_add_u32 s98, s4, 0x0
	s_addc_u32 s99, s5, 0
	global_load_dwordx4 v[154:157], v248, s[98:99]
	global_load_dwordx4 v[158:161], v248, s[98:99] offset:64
	global_load_dwordx4 v[162:165], v248, s[98:99] offset:512
	global_load_dwordx4 v[166:169], v248, s[98:99] offset:576
	s_add_u32 s98, s4, 0x20000
	s_addc_u32 s99, s5, 0
	global_load_dwordx4 v[170:173], v248, s[98:99]
	global_load_dwordx4 v[174:177], v248, s[98:99] offset:64
	global_load_dwordx4 v[178:181], v248, s[98:99] offset:512
	global_load_dwordx4 v[182:185], v248, s[98:99] offset:576
	s_add_u32 s98, s4, 0x40000
	s_addc_u32 s99, s5, 0
	global_load_dwordx4 v[186:189], v248, s[98:99]
	global_load_dwordx4 v[190:193], v248, s[98:99] offset:64
	global_load_dwordx4 v[194:197], v248, s[98:99] offset:512
	global_load_dwordx4 v[198:201], v248, s[98:99] offset:576
	s_add_u32 s98, s4, 0x60000
	s_addc_u32 s99, s5, 0
	global_load_dwordx4 v[202:205], v248, s[98:99]
	global_load_dwordx4 v[206:209], v248, s[98:99] offset:64
	global_load_dwordx4 v[210:213], v248, s[98:99] offset:512
	global_load_dwordx4 v[214:217], v248, s[98:99] offset:576
	s_add_u32 s100, s6, 0x0
	s_addc_u32 s101, s7, 0
	s_add_u32 s98, s4, 0x100000
	s_addc_u32 s99, s5, 0
	s_waitcnt vmcnt(15)
	v_pk_add_f32 v[154:155], v[124:125], v[154:155]
	v_pk_add_f32 v[156:157], v[126:127], v[156:157]
	global_store_dwordx4 v248, v[154:157], s[100:101]
	s_nop 1
	global_load_dwordx4 v[154:157], v248, s[98:99]
	s_waitcnt vmcnt(16)
	v_pk_add_f32 v[158:159], v[120:121], v[158:159]
	v_pk_add_f32 v[160:161], v[122:123], v[160:161]
	global_store_dwordx4 v248, v[158:161], s[100:101] offset:64
	s_nop 1
	global_load_dwordx4 v[158:161], v248, s[98:99] offset:64
	s_waitcnt vmcnt(17)
	v_pk_add_f32 v[162:163], v[116:117], v[162:163]
	v_pk_add_f32 v[164:165], v[118:119], v[164:165]
	global_store_dwordx4 v248, v[162:165], s[100:101] offset:512
	s_nop 1
	global_load_dwordx4 v[162:165], v248, s[98:99] offset:512
	s_waitcnt vmcnt(18)
	v_pk_add_f32 v[166:167], v[104:105], v[166:167]
	v_pk_add_f32 v[168:169], v[106:107], v[168:169]
	global_store_dwordx4 v248, v[166:169], s[100:101] offset:576
	s_nop 1
	global_load_dwordx4 v[166:169], v248, s[98:99] offset:576
	s_add_u32 s100, s6, 0x20000
	s_addc_u32 s101, s7, 0
	s_add_u32 s98, s4, 0x120000
	s_addc_u32 s99, s5, 0
	s_waitcnt vmcnt(19)
	v_pk_add_f32 v[170:171], v[112:113], v[170:171]
	v_pk_add_f32 v[172:173], v[114:115], v[172:173]
	global_store_dwordx4 v248, v[170:173], s[100:101]
	s_nop 1
	global_load_dwordx4 v[170:173], v248, s[98:99]
	s_waitcnt vmcnt(20)
	v_pk_add_f32 v[174:175], v[108:109], v[174:175]
	v_pk_add_f32 v[176:177], v[110:111], v[176:177]
	global_store_dwordx4 v248, v[174:177], s[100:101] offset:64
	s_nop 1
	global_load_dwordx4 v[174:177], v248, s[98:99] offset:64
	s_waitcnt vmcnt(21)
	v_pk_add_f32 v[178:179], v[100:101], v[178:179]
	v_pk_add_f32 v[180:181], v[102:103], v[180:181]
	global_store_dwordx4 v248, v[178:181], s[100:101] offset:512
	s_nop 1
	global_load_dwordx4 v[178:181], v248, s[98:99] offset:512
	s_waitcnt vmcnt(22)
	v_pk_add_f32 v[182:183], v[88:89], v[182:183]
	v_pk_add_f32 v[184:185], v[90:91], v[184:185]
	global_store_dwordx4 v248, v[182:185], s[100:101] offset:576
	s_nop 1
	global_load_dwordx4 v[182:185], v248, s[98:99] offset:576
	s_add_u32 s100, s6, 0x40000
	s_addc_u32 s101, s7, 0
	s_add_u32 s98, s4, 0x140000
	s_addc_u32 s99, s5, 0
	s_waitcnt vmcnt(23)
	v_pk_add_f32 v[186:187], v[96:97], v[186:187]
	v_pk_add_f32 v[188:189], v[98:99], v[188:189]
	global_store_dwordx4 v248, v[186:189], s[100:101]
	s_nop 1
	global_load_dwordx4 v[186:189], v248, s[98:99]
	s_waitcnt vmcnt(24)
	v_pk_add_f32 v[190:191], v[92:93], v[190:191]
	v_pk_add_f32 v[192:193], v[94:95], v[192:193]
	global_store_dwordx4 v248, v[190:193], s[100:101] offset:64
	s_nop 1
	global_load_dwordx4 v[190:193], v248, s[98:99] offset:64
	s_waitcnt vmcnt(25)
	v_pk_add_f32 v[194:195], v[84:85], v[194:195]
	v_pk_add_f32 v[196:197], v[86:87], v[196:197]
	global_store_dwordx4 v248, v[194:197], s[100:101] offset:512
	s_nop 1
	global_load_dwordx4 v[194:197], v248, s[98:99] offset:512
	s_waitcnt vmcnt(26)
	v_pk_add_f32 v[198:199], v[72:73], v[198:199]
	v_pk_add_f32 v[200:201], v[74:75], v[200:201]
	global_store_dwordx4 v248, v[198:201], s[100:101] offset:576
	s_nop 1
	global_load_dwordx4 v[198:201], v248, s[98:99] offset:576
	s_add_u32 s100, s6, 0x60000
	s_addc_u32 s101, s7, 0
	s_add_u32 s98, s4, 0x160000
	s_addc_u32 s99, s5, 0
	s_waitcnt vmcnt(27)
	v_pk_add_f32 v[202:203], v[80:81], v[202:203]
	v_pk_add_f32 v[204:205], v[82:83], v[204:205]
	global_store_dwordx4 v248, v[202:205], s[100:101]
	s_nop 1
	global_load_dwordx4 v[202:205], v248, s[98:99]
	s_waitcnt vmcnt(28)
	v_pk_add_f32 v[206:207], v[76:77], v[206:207]
	v_pk_add_f32 v[208:209], v[78:79], v[208:209]
	global_store_dwordx4 v248, v[206:209], s[100:101] offset:64
	s_nop 1
	global_load_dwordx4 v[206:209], v248, s[98:99] offset:64
	s_waitcnt vmcnt(29)
	v_pk_add_f32 v[210:211], v[64:65], v[210:211]
	v_pk_add_f32 v[212:213], v[66:67], v[212:213]
	global_store_dwordx4 v248, v[210:213], s[100:101] offset:512
	s_nop 1
	global_load_dwordx4 v[210:213], v248, s[98:99] offset:512
	s_waitcnt vmcnt(30)
	v_pk_add_f32 v[214:215], v[56:57], v[214:215]
	v_pk_add_f32 v[216:217], v[58:59], v[216:217]
	global_store_dwordx4 v248, v[214:217], s[100:101] offset:576
	s_nop 1
	global_load_dwordx4 v[214:217], v248, s[98:99] offset:576
	s_add_u32 s100, s6, 0x100000
	s_addc_u32 s101, s7, 0
	s_waitcnt vmcnt(30)
	v_pk_add_f32 v[154:155], v[52:53], v[154:155]
	v_pk_add_f32 v[156:157], v[54:55], v[156:157]
	global_store_dwordx4 v248, v[154:157], s[100:101]
	s_waitcnt vmcnt(29)
	v_pk_add_f32 v[158:159], v[44:45], v[158:159]
	v_pk_add_f32 v[160:161], v[46:47], v[160:161]
	global_store_dwordx4 v248, v[158:161], s[100:101] offset:64
	s_waitcnt vmcnt(28)
	v_pk_add_f32 v[162:163], v[68:69], v[162:163]
	v_pk_add_f32 v[164:165], v[70:71], v[164:165]
	global_store_dwordx4 v248, v[162:165], s[100:101] offset:512
	s_waitcnt vmcnt(27)
	v_pk_add_f32 v[166:167], v[60:61], v[166:167]
	v_pk_add_f32 v[168:169], v[62:63], v[168:169]
	global_store_dwordx4 v248, v[166:169], s[100:101] offset:576
	s_add_u32 s100, s6, 0x120000
	s_addc_u32 s101, s7, 0
	s_waitcnt vmcnt(26)
	v_pk_add_f32 v[170:171], v[32:33], v[170:171]
	v_pk_add_f32 v[172:173], v[34:35], v[172:173]
	global_store_dwordx4 v248, v[170:173], s[100:101]
	s_waitcnt vmcnt(25)
	v_pk_add_f32 v[174:175], v[24:25], v[174:175]
	v_pk_add_f32 v[176:177], v[26:27], v[176:177]
	global_store_dwordx4 v248, v[174:177], s[100:101] offset:64
	s_waitcnt vmcnt(24)
	v_pk_add_f32 v[178:179], v[48:49], v[178:179]
	v_pk_add_f32 v[180:181], v[50:51], v[180:181]
	global_store_dwordx4 v248, v[178:181], s[100:101] offset:512
	s_waitcnt vmcnt(23)
	v_pk_add_f32 v[182:183], v[40:41], v[182:183]
	v_pk_add_f32 v[184:185], v[42:43], v[184:185]
	global_store_dwordx4 v248, v[182:185], s[100:101] offset:576
	s_add_u32 s100, s6, 0x140000
	s_addc_u32 s101, s7, 0
	s_waitcnt vmcnt(22)
	v_pk_add_f32 v[186:187], v[12:13], v[186:187]
	v_pk_add_f32 v[188:189], v[14:15], v[188:189]
	global_store_dwordx4 v248, v[186:189], s[100:101]
	s_waitcnt vmcnt(21)
	v_pk_add_f32 v[190:191], v[8:9], v[190:191]
	v_pk_add_f32 v[192:193], v[10:11], v[192:193]
	global_store_dwordx4 v248, v[190:193], s[100:101] offset:64
	s_waitcnt vmcnt(20)
	v_pk_add_f32 v[194:195], v[36:37], v[194:195]
	v_pk_add_f32 v[196:197], v[38:39], v[196:197]
	global_store_dwordx4 v248, v[194:197], s[100:101] offset:512
	s_waitcnt vmcnt(19)
	v_pk_add_f32 v[198:199], v[28:29], v[198:199]
	v_pk_add_f32 v[200:201], v[30:31], v[200:201]
	global_store_dwordx4 v248, v[198:201], s[100:101] offset:576
	s_add_u32 s100, s6, 0x160000
	s_addc_u32 s101, s7, 0
	s_waitcnt vmcnt(18)
	v_pk_add_f32 v[202:203], v[4:5], v[202:203]
	v_pk_add_f32 v[204:205], v[6:7], v[204:205]
	global_store_dwordx4 v248, v[202:205], s[100:101]
	s_waitcnt vmcnt(17)
	v_pk_add_f32 v[206:207], v[0:1], v[206:207]
	v_pk_add_f32 v[208:209], v[2:3], v[208:209]
	global_store_dwordx4 v248, v[206:209], s[100:101] offset:64
	s_waitcnt vmcnt(16)
	v_pk_add_f32 v[210:211], v[20:21], v[210:211]
	v_pk_add_f32 v[212:213], v[22:23], v[212:213]
	global_store_dwordx4 v248, v[210:213], s[100:101] offset:512
	s_waitcnt vmcnt(15)
	v_pk_add_f32 v[214:215], v[16:17], v[214:215]
	v_pk_add_f32 v[216:217], v[18:19], v[216:217]
	global_store_dwordx4 v248, v[214:217], s[100:101] offset:576
	s_cbranch_vccnz .LBB0_877
	s_andn2_b64 vcc, exec, s[8:9]
	s_cbranch_vccnz .LBB0_876
	s_barrier
	s_branch .LBB0_876

.LBB0_2246:
	v_lshl_add_u32 v148, s28, 8, v150
	v_lshl_or_b32 v144, s29, 8, v151
	v_lshlrev_b32_e32 v248, 13, v148
	v_lshl_add_u32 v248, v144, 2, v248
	s_mov_b64 s[28:29], -1
	s_andn2_b64 vcc, exec, s[2:3]
	s_add_u32 s98, s4, 0x0
	s_addc_u32 s99, s5, 0
	global_load_dwordx4 v[144:147], v248, s[98:99]
	global_load_dwordx4 v[158:161], v248, s[98:99] offset:64
	global_load_dwordx4 v[162:165], v248, s[98:99] offset:512
	global_load_dwordx4 v[166:169], v248, s[98:99] offset:576
	s_add_u32 s98, s4, 0x20000
	s_addc_u32 s99, s5, 0
	global_load_dwordx4 v[170:173], v248, s[98:99]
	global_load_dwordx4 v[174:177], v248, s[98:99] offset:64
	global_load_dwordx4 v[178:181], v248, s[98:99] offset:512
	global_load_dwordx4 v[182:185], v248, s[98:99] offset:576
	s_add_u32 s98, s4, 0x40000
	s_addc_u32 s99, s5, 0
	global_load_dwordx4 v[186:189], v248, s[98:99]
	global_load_dwordx4 v[190:193], v248, s[98:99] offset:64
	global_load_dwordx4 v[194:197], v248, s[98:99] offset:512
	global_load_dwordx4 v[198:201], v248, s[98:99] offset:576
	s_add_u32 s98, s4, 0x60000
	s_addc_u32 s99, s5, 0
	global_load_dwordx4 v[202:205], v248, s[98:99]
	global_load_dwordx4 v[206:209], v248, s[98:99] offset:64
	global_load_dwordx4 v[210:213], v248, s[98:99] offset:512
	global_load_dwordx4 v[214:217], v248, s[98:99] offset:576
	s_add_u32 s100, s4, 0x0
	s_addc_u32 s101, s5, 0
	s_add_u32 s98, s4, 0x100000
	s_addc_u32 s99, s5, 0
	s_waitcnt vmcnt(15)
	v_pk_add_f32 v[144:145], v[124:125], v[144:145]
	v_pk_add_f32 v[146:147], v[126:127], v[146:147]
	global_store_dwordx4 v248, v[144:147], s[100:101]
	s_nop 1
	global_load_dwordx4 v[144:147], v248, s[98:99]
	s_waitcnt vmcnt(16)
	v_pk_add_f32 v[158:159], v[120:121], v[158:159]
	v_pk_add_f32 v[160:161], v[122:123], v[160:161]
	global_store_dwordx4 v248, v[158:161], s[100:101] offset:64
	s_nop 1
	global_load_dwordx4 v[158:161], v248, s[98:99] offset:64
	s_waitcnt vmcnt(17)
	v_pk_add_f32 v[162:163], v[116:117], v[162:163]
	v_pk_add_f32 v[164:165], v[118:119], v[164:165]
	global_store_dwordx4 v248, v[162:165], s[100:101] offset:512
	s_nop 1
	global_load_dwordx4 v[162:165], v248, s[98:99] offset:512
	s_waitcnt vmcnt(18)
	v_pk_add_f32 v[166:167], v[108:109], v[166:167]
	v_pk_add_f32 v[168:169], v[110:111], v[168:169]
	global_store_dwordx4 v248, v[166:169], s[100:101] offset:576
	s_nop 1
	global_load_dwordx4 v[166:169], v248, s[98:99] offset:576
	s_add_u32 s100, s4, 0x20000
	s_addc_u32 s101, s5, 0
	s_add_u32 s98, s4, 0x120000
	s_addc_u32 s99, s5, 0
	s_waitcnt vmcnt(19)
	v_pk_add_f32 v[170:171], v[112:113], v[170:171]
	v_pk_add_f32 v[172:173], v[114:115], v[172:173]
	global_store_dwordx4 v248, v[170:173], s[100:101]
	s_nop 1
	global_load_dwordx4 v[170:173], v248, s[98:99]
	s_waitcnt vmcnt(20)
	v_pk_add_f32 v[174:175], v[104:105], v[174:175]
	v_pk_add_f32 v[176:177], v[106:107], v[176:177]
	global_store_dwordx4 v248, v[174:177], s[100:101] offset:64
	s_nop 1
	global_load_dwordx4 v[174:177], v248, s[98:99] offset:64
	s_waitcnt vmcnt(21)
	v_pk_add_f32 v[178:179], v[100:101], v[178:179]
	v_pk_add_f32 v[180:181], v[102:103], v[180:181]
	global_store_dwordx4 v248, v[178:181], s[100:101] offset:512
	s_nop 1
	global_load_dwordx4 v[178:181], v248, s[98:99] offset:512
	s_waitcnt vmcnt(22)
	v_pk_add_f32 v[182:183], v[96:97], v[182:183]
	v_pk_add_f32 v[184:185], v[98:99], v[184:185]
	global_store_dwordx4 v248, v[182:185], s[100:101] offset:576
	s_nop 1
	global_load_dwordx4 v[182:185], v248, s[98:99] offset:576
	s_add_u32 s100, s4, 0x40000
	s_addc_u32 s101, s5, 0
	s_add_u32 s98, s4, 0x140000
	s_addc_u32 s99, s5, 0
	s_waitcnt vmcnt(23)
	v_pk_add_f32 v[186:187], v[92:93], v[186:187]
	v_pk_add_f32 v[188:189], v[94:95], v[188:189]
	global_store_dwordx4 v248, v[186:189], s[100:101]
	s_nop 1
	global_load_dwordx4 v[186:189], v248, s[98:99]
	s_waitcnt vmcnt(24)
	v_pk_add_f32 v[190:191], v[88:89], v[190:191]
	v_pk_add_f32 v[192:193], v[90:91], v[192:193]
	global_store_dwordx4 v248, v[190:193], s[100:101] offset:64
	s_nop 1
	global_load_dwordx4 v[190:193], v248, s[98:99] offset:64
	s_waitcnt vmcnt(25)
	v_pk_add_f32 v[194:195], v[84:85], v[194:195]
	v_pk_add_f32 v[196:197], v[86:87], v[196:197]
	global_store_dwordx4 v248, v[194:197], s[100:101] offset:512
	s_nop 1
	global_load_dwordx4 v[194:197], v248, s[98:99] offset:512
	s_waitcnt vmcnt(26)
	v_pk_add_f32 v[198:199], v[80:81], v[198:199]
	v_pk_add_f32 v[200:201], v[82:83], v[200:201]
	global_store_dwordx4 v248, v[198:201], s[100:101] offset:576
	s_nop 1
	global_load_dwordx4 v[198:201], v248, s[98:99] offset:576
	s_add_u32 s100, s4, 0x60000
	s_addc_u32 s101, s5, 0
	s_add_u32 s98, s4, 0x160000
	s_addc_u32 s99, s5, 0
	s_waitcnt vmcnt(27)
	v_pk_add_f32 v[202:203], v[76:77], v[202:203]
	v_pk_add_f32 v[204:205], v[78:79], v[204:205]
	global_store_dwordx4 v248, v[202:205], s[100:101]
	s_nop 1
	global_load_dwordx4 v[202:205], v248, s[98:99]
	s_waitcnt vmcnt(28)
	v_pk_add_f32 v[206:207], v[72:73], v[206:207]
	v_pk_add_f32 v[208:209], v[74:75], v[208:209]
	global_store_dwordx4 v248, v[206:209], s[100:101] offset:64
	s_nop 1
	global_load_dwordx4 v[206:209], v248, s[98:99] offset:64
	s_waitcnt vmcnt(29)
	v_pk_add_f32 v[210:211], v[68:69], v[210:211]
	v_pk_add_f32 v[212:213], v[70:71], v[212:213]
	global_store_dwordx4 v248, v[210:213], s[100:101] offset:512
	s_nop 1
	global_load_dwordx4 v[210:213], v248, s[98:99] offset:512
	s_waitcnt vmcnt(30)
	v_pk_add_f32 v[214:215], v[64:65], v[214:215]
	v_pk_add_f32 v[216:217], v[66:67], v[216:217]
	global_store_dwordx4 v248, v[214:217], s[100:101] offset:576
	s_nop 1
	global_load_dwordx4 v[214:217], v248, s[98:99] offset:576
	s_add_u32 s100, s4, 0x100000
	s_addc_u32 s101, s5, 0
	s_waitcnt vmcnt(30)
	v_pk_add_f32 v[144:145], v[52:53], v[144:145]
	v_pk_add_f32 v[146:147], v[54:55], v[146:147]
	global_store_dwordx4 v248, v[144:147], s[100:101]
	s_waitcnt vmcnt(29)
	v_pk_add_f32 v[158:159], v[48:49], v[158:159]
	v_pk_add_f32 v[160:161], v[50:51], v[160:161]
	global_store_dwordx4 v248, v[158:161], s[100:101] offset:64
	s_waitcnt vmcnt(28)
	v_pk_add_f32 v[162:163], v[56:57], v[162:163]
	v_pk_add_f32 v[164:165], v[58:59], v[164:165]
	global_store_dwordx4 v248, v[162:165], s[100:101] offset:512
	s_waitcnt vmcnt(27)
	v_pk_add_f32 v[166:167], v[60:61], v[166:167]
	v_pk_add_f32 v[168:169], v[62:63], v[168:169]
	global_store_dwordx4 v248, v[166:169], s[100:101] offset:576
	s_add_u32 s100, s4, 0x120000
	s_addc_u32 s101, s5, 0
	s_waitcnt vmcnt(26)
	v_pk_add_f32 v[170:171], v[36:37], v[170:171]
	v_pk_add_f32 v[172:173], v[38:39], v[172:173]
	global_store_dwordx4 v248, v[170:173], s[100:101]
	s_waitcnt vmcnt(25)
	v_pk_add_f32 v[174:175], v[32:33], v[174:175]
	v_pk_add_f32 v[176:177], v[34:35], v[176:177]
	global_store_dwordx4 v248, v[174:177], s[100:101] offset:64
	s_waitcnt vmcnt(24)
	v_pk_add_f32 v[178:179], v[40:41], v[178:179]
	v_pk_add_f32 v[180:181], v[42:43], v[180:181]
	global_store_dwordx4 v248, v[178:181], s[100:101] offset:512
	s_waitcnt vmcnt(23)
	v_pk_add_f32 v[182:183], v[44:45], v[182:183]
	v_pk_add_f32 v[184:185], v[46:47], v[184:185]
	global_store_dwordx4 v248, v[182:185], s[100:101] offset:576
	s_add_u32 s100, s4, 0x140000
	s_addc_u32 s101, s5, 0
	s_waitcnt vmcnt(22)
	v_pk_add_f32 v[186:187], v[20:21], v[186:187]
	v_pk_add_f32 v[188:189], v[22:23], v[188:189]
	global_store_dwordx4 v248, v[186:189], s[100:101]
	s_waitcnt vmcnt(21)
	v_pk_add_f32 v[190:191], v[16:17], v[190:191]
	v_pk_add_f32 v[192:193], v[18:19], v[192:193]
	global_store_dwordx4 v248, v[190:193], s[100:101] offset:64
	s_waitcnt vmcnt(20)
	v_pk_add_f32 v[194:195], v[28:29], v[194:195]
	v_pk_add_f32 v[196:197], v[30:31], v[196:197]
	global_store_dwordx4 v248, v[194:197], s[100:101] offset:512
	s_waitcnt vmcnt(19)
	v_pk_add_f32 v[198:199], v[24:25], v[198:199]
	v_pk_add_f32 v[200:201], v[26:27], v[200:201]
	global_store_dwordx4 v248, v[198:201], s[100:101] offset:576
	s_add_u32 s100, s4, 0x160000
	s_addc_u32 s101, s5, 0
	s_waitcnt vmcnt(18)
	v_pk_add_f32 v[202:203], v[8:9], v[202:203]
	v_pk_add_f32 v[204:205], v[10:11], v[204:205]
	global_store_dwordx4 v248, v[202:205], s[100:101]
	s_waitcnt vmcnt(17)
	v_pk_add_f32 v[206:207], v[4:5], v[206:207]
	v_pk_add_f32 v[208:209], v[6:7], v[208:209]
	global_store_dwordx4 v248, v[206:209], s[100:101] offset:64
	s_waitcnt vmcnt(16)
	v_pk_add_f32 v[210:211], v[12:13], v[210:211]
	v_pk_add_f32 v[212:213], v[14:15], v[212:213]
	global_store_dwordx4 v248, v[210:213], s[100:101] offset:512
	s_waitcnt vmcnt(15)
	v_pk_add_f32 v[214:215], v[0:1], v[214:215]
	v_pk_add_f32 v[216:217], v[2:3], v[216:217]
	global_store_dwordx4 v248, v[214:217], s[100:101] offset:576
	s_cbranch_vccnz .LBB0_2235
	s_andn2_b64 vcc, exec, s[6:7]
	s_cbranch_vccnz .LBB0_2234
	s_barrier
	s_branch .LBB0_2234

	.amdhsa_kernel _Z10fwd_kernelILin1EEv4Args
		.amdhsa_group_segment_fixed_size 0
		.amdhsa_private_segment_fixed_size 0
		.amdhsa_kernarg_size 512
		.amdhsa_user_sgpr_count 2
		.amdhsa_user_sgpr_dispatch_ptr 0
		.amdhsa_user_sgpr_queue_ptr 0
		.amdhsa_user_sgpr_kernarg_segment_ptr 1
		.amdhsa_user_sgpr_dispatch_id 0
		.amdhsa_user_sgpr_kernarg_preload_length 0
		.amdhsa_user_sgpr_kernarg_preload_offset 0
		.amdhsa_user_sgpr_private_segment_size 0
		.amdhsa_uses_dynamic_stack 0
		.amdhsa_enable_private_segment 0
		.amdhsa_system_sgpr_workgroup_id_x 1
		.amdhsa_system_sgpr_workgroup_id_y 0
		.amdhsa_system_sgpr_workgroup_id_z 0
		.amdhsa_system_sgpr_workgroup_info 0
		.amdhsa_system_vgpr_workitem_id 0
		.amdhsa_next_free_vgpr 252
		.amdhsa_next_free_sgpr 102
		.amdhsa_accum_offset 252
		.amdhsa_reserve_vcc 1
		.amdhsa_float_round_mode_32 0
		.amdhsa_float_round_mode_16_64 0
		.amdhsa_float_denorm_mode_32 3
		.amdhsa_float_denorm_mode_16_64 3
		.amdhsa_dx10_clamp 1
		.amdhsa_ieee_mode 1
		.amdhsa_fp16_overflow 0
		.amdhsa_tg_split 0
		.amdhsa_exception_fp_ieee_invalid_op 0
		.amdhsa_exception_fp_denorm_src 0
		.amdhsa_exception_fp_ieee_div_zero 0
		.amdhsa_exception_fp_ieee_overflow 0
		.amdhsa_exception_fp_ieee_underflow 0
		.amdhsa_exception_fp_ieee_inexact 0
		.amdhsa_exception_int_div_zero 0
	.end_amdhsa_kernel

amdhsa.kernels:
  - .agpr_count:     0
    .args:
      - .offset:         0
        .size:           256
        .value_kind:     by_value
      - .offset:         256
        .size:           4
        .value_kind:     hidden_block_count_x
      - .offset:         260
        .size:           4
        .value_kind:     hidden_block_count_y
      - .offset:         264
        .size:           4
        .value_kind:     hidden_block_count_z
      - .offset:         268
        .size:           2
        .value_kind:     hidden_group_size_x
      - .offset:         270
        .size:           2
        .value_kind:     hidden_group_size_y
      - .offset:         272
        .size:           2
        .value_kind:     hidden_group_size_z
      - .offset:         274
        .size:           2
        .value_kind:     hidden_remainder_x
      - .offset:         276
        .size:           2
        .value_kind:     hidden_remainder_y
      - .offset:         278
        .size:           2
        .value_kind:     hidden_remainder_z
      - .offset:         296
        .size:           8
        .value_kind:     hidden_global_offset_x
      - .offset:         304
        .size:           8
        .value_kind:     hidden_global_offset_y
      - .offset:         312
        .size:           8
        .value_kind:     hidden_global_offset_z
      - .offset:         320
        .size:           2
        .value_kind:     hidden_grid_dims
      - .offset:         376
        .size:           4
        .value_kind:     hidden_dynamic_lds_size
    .group_segment_fixed_size: 0
    .kernarg_segment_align: 8
    .kernarg_segment_size: 512
    .language:       OpenCL C
    .language_version:
      - 2
      - 0
    .max_flat_workgroup_size: 512
    .name:           _Z10fwd_kernelILin1EEv4Args
    .private_segment_fixed_size: 0
    .sgpr_count:     108
    .sgpr_spill_count: 2
    .symbol:         _Z10fwd_kernelILin1EEv4Args.kd
    .uniform_work_group_size: 1
    .uses_dynamic_stack: false
    .vgpr_count:     252
    .vgpr_spill_count: 0
    .wavefront_size: 64
